# xattn: both staging batches of K and V^T in flight together
# baseline (speedup 1.0000x reference)
.LBB0_1221:
	v_mov_b64_e32 v[4:5], 0x200
	v_cmp_lt_i64_e32 vcc, s[4:5], v[4:5]
	s_mov_b64 s[4:5], -1
	s_cbranch_vccz .LBB0_1214
	v_readlane_b32 s7, v255, 58
	s_ashr_i32 s20, s7, 4
	v_readfirstlane_b32 s6, v173
	s_lshl_b32 s7, s7, 8
	s_ashr_i32 s21, s20, 31
	s_and_b32 s9, s7, 0xf00
	s_ashr_i32 s6, s6, 1
	s_lshl_b64 s[4:5], s[20:21], 12
	s_andn2_b32 s6, s6, 31
	v_or_b32_e32 v4, s9, v176
	s_ashr_i32 s7, s6, 31
	v_or_b32_e32 v4, s4, v4
	v_mov_b32_e32 v5, s5
	v_lshl_add_u64 v[4:5], v[4:5], 0, s[6:7]
	v_lshlrev_b64 v[6:7], 6, v[4:5]
	v_lshl_add_u64 v[18:19], s[14:15], 0, v[6:7]
	global_load_dwordx4 v[6:9], v[18:19], off offset:48
	global_load_dwordx4 v[10:13], v[18:19], off offset:32
	global_load_dwordx4 v[14:17], v[18:19], off offset:16
	s_nop 0
	global_load_dwordx4 v[18:21], v[18:19], off
	v_lshlrev_b64 v[170:171], 11, v[4:5]
	v_lshl_add_u64 v[4:5], s[10:11], 0, v[170:171]
	s_waitcnt vmcnt(2)
	v_add_f32_e32 v10, v10, v11
	v_add_f32_e32 v12, v12, v13
	s_waitcnt vmcnt(0)
	v_mov_b32_e32 v22, v19
	v_mov_b32_e32 v23, v20
	v_mov_b32_e32 v19, v21
	v_mov_b32_e32 v20, v15
	v_mov_b32_e32 v21, v16
	v_mov_b32_e32 v15, v17
	v_pk_add_f32 v[18:19], v[22:23], v[18:19]
	v_pk_add_f32 v[14:15], v[20:21], v[14:15]
	v_pk_add_f32 v[18:19], v[18:19], v[18:19] op_sel:[0,1] op_sel_hi:[1,0]
	v_pk_add_f32 v[14:15], v[14:15], v[14:15] op_sel:[0,1] op_sel_hi:[1,0]
	v_mov_b32_e32 v19, v6
	v_mov_b32_e32 v15, v7
	v_mov_b32_e32 v11, v8
	v_mov_b32_e32 v13, v9
	v_pk_add_f32 v[6:7], v[18:19], v[14:15]
	v_pk_add_f32 v[8:9], v[10:11], v[12:13]
	s_nop 0
	v_pk_add_f32 v[6:7], v[6:7], v[8:9]
	s_nop 0
	v_add_f32_e32 v6, v6, v7
	v_fmamk_f32 v6, v6, 0x3a800000, v1
	v_cmp_gt_f32_e32 vcc, s29, v6
	v_mul_f32_e32 v7, 0x4f800000, v6
	s_nop 0
	v_cndmask_b32_e32 v6, v6, v7, vcc
	v_sqrt_f32_e32 v7, v6
	s_nop 0
	v_add_u32_e32 v8, -1, v7
	v_fma_f32 v9, -v8, v7, v6
	v_cmp_ge_f32_e64 s[38:39], 0, v9
	v_add_u32_e32 v9, 1, v7
	s_nop 0
	v_cndmask_b32_e64 v8, v7, v8, s[38:39]
	v_fma_f32 v7, -v9, v7, v6
	v_cmp_lt_f32_e64 s[38:39], 0, v7
	s_nop 1
	v_cndmask_b32_e64 v7, v8, v9, s[38:39]
	v_mul_f32_e32 v8, 0x37800000, v7
	v_cndmask_b32_e32 v7, v7, v8, vcc
	v_cmp_class_f32_e32 vcc, v6, v248
	s_nop 1
	v_cndmask_b32_e32 v6, v7, v6, vcc
	v_div_scale_f32 v7, s[4:5], v6, v6, 1.0
	v_rcp_f32_e32 v8, v7
	v_readlane_b32 s4, v255, 57
	s_lshl_b32 s22, s4, 8
	s_ashr_i32 s23, s22, 31
	v_fma_f32 v9, -v7, v8, 1.0
	v_fmac_f32_e32 v8, v9, v8
	v_div_scale_f32 v9, vcc, 1.0, v6, 1.0
	v_mul_f32_e32 v10, v9, v8
	v_fma_f32 v11, -v7, v10, v9
	s_lshl_b32 s4, s20, 8
	v_fmac_f32_e32 v10, v11, v8
	s_lshl_b64 s[18:19], s[22:23], 1
	s_ashr_i32 s5, s4, 31
	v_fma_f32 v7, -v7, v10, v9
	v_lshl_add_u64 v[38:39], v[148:149], 0, s[18:19]
	s_lshl_b64 s[6:7], s[4:5], 11
	v_div_fmas_f32 v7, v7, v8, v10
	v_lshl_add_u64 v[18:19], v[38:39], 0, s[6:7]
	v_div_fixup_f32 v42, v7, v6, 1.0
	v_lshl_add_u64 v[6:7], v[18:19], 0, v[150:151]
	s_or_b32 s6, s4, 64
	global_load_dwordx4 v[6:9], v[6:7], off
	v_lshl_add_u64 v[10:11], v[18:19], 0, v[152:153]
	s_ashr_i32 s7, s6, 31
	global_load_dwordx4 v[10:13], v[10:11], off
	v_lshl_add_u64 v[14:15], v[18:19], 0, v[154:155]
	s_lshl_b64 s[6:7], s[6:7], 11
	global_load_dwordx4 v[14:17], v[14:15], off
	v_lshl_add_u64 v[18:19], v[18:19], 0, v[156:157]
	v_lshl_add_u64 v[34:35], v[38:39], 0, s[6:7]
	global_load_dwordx4 v[18:21], v[18:19], off
	v_lshl_add_u64 v[22:23], v[34:35], 0, v[150:151]
	global_load_dwordx4 v[22:25], v[22:23], off
	v_lshl_add_u64 v[26:27], v[34:35], 0, v[152:153]
	global_load_dwordx4 v[26:29], v[26:27], off
	v_lshl_add_u64 v[30:31], v[34:35], 0, v[154:155]
	global_load_dwordx4 v[30:33], v[30:31], off
	v_lshl_add_u64 v[34:35], v[34:35], 0, v[156:157]
	global_load_dwordx4 v[34:37], v[34:35], off
	s_or_b32 s6, s4, 0x80
	s_ashr_i32 s7, s6, 31
	s_lshl_b64 s[6:7], s[6:7], 11
	v_lshl_add_u64 v[40:41], v[4:5], 0, s[18:19]
	s_or_b32 s4, s4, 0xc0
	s_ashr_i32 s5, s4, 31
	s_lshl_b64 s[4:5], s[4:5], 11
	v_lshl_add_u64 v[174:175], v[40:41], 0, v[2:3]
	v_mul_f32_e32 v172, 0x3db8aa3b, v42
	v_lshl_add_u64 v[220:221], v[38:39], 0, s[6:7]
	v_lshl_add_u64 v[208:209], v[220:221], 0, v[150:151]
	global_load_dwordx4 v[208:211], v[208:209], off
	v_lshl_add_u64 v[212:213], v[220:221], 0, v[152:153]
	global_load_dwordx4 v[212:215], v[212:213], off
	v_lshl_add_u64 v[216:217], v[220:221], 0, v[154:155]
	global_load_dwordx4 v[216:219], v[216:217], off
	v_lshl_add_u64 v[220:221], v[220:221], 0, v[156:157]
	v_lshl_add_u64 v[236:237], v[38:39], 0, s[4:5]
	global_load_dwordx4 v[220:223], v[220:221], off
	v_lshl_add_u64 v[224:225], v[236:237], 0, v[150:151]
	global_load_dwordx4 v[224:227], v[224:225], off
	v_lshl_add_u64 v[228:229], v[236:237], 0, v[152:153]
	global_load_dwordx4 v[228:231], v[228:229], off
	v_lshl_add_u64 v[232:233], v[236:237], 0, v[154:155]
	global_load_dwordx4 v[232:235], v[232:233], off
	v_lshl_add_u64 v[236:237], v[236:237], 0, v[156:157]
	global_load_dwordx4 v[236:239], v[236:237], off
	s_lshl_b32 s4, s20, 10
	s_add_i32 s4, s22, s4
	s_ashr_i32 s5, s4, 31
	s_lshl_b64 s[12:13], s[4:5], 9
	s_mov_b32 s6, 0
	s_waitcnt vmcnt(15)
	ds_write_b128 v179, v[6:9]
	s_waitcnt vmcnt(14)
	ds_write_b128 v179, v[10:13] offset:8448
	s_waitcnt vmcnt(13)
	ds_write_b128 v179, v[14:17] offset:16896
	s_waitcnt vmcnt(12)
	ds_write_b128 v179, v[18:21] offset:25344
	s_waitcnt vmcnt(11)
	ds_write_b128 v179, v[22:25] offset:33792
	s_waitcnt vmcnt(10)
	ds_write_b128 v179, v[26:29] offset:42240
	s_waitcnt vmcnt(9)
	ds_write_b128 v179, v[30:33] offset:50688
	s_waitcnt vmcnt(8)
	ds_write_b128 v179, v[34:37] offset:59136
	s_waitcnt vmcnt(7)
	ds_write_b128 v180, v[208:211]
	s_waitcnt vmcnt(6)
	ds_write_b128 v180, v[212:215] offset:8448
	s_waitcnt vmcnt(5)
	ds_write_b128 v180, v[216:219] offset:16896
	s_waitcnt vmcnt(4)
	ds_write_b128 v180, v[220:223] offset:25344
	s_waitcnt vmcnt(3)
	ds_write_b128 v181, v[224:227]
	s_waitcnt vmcnt(2)
	ds_write_b128 v181, v[228:231] offset:8448
	s_waitcnt vmcnt(1)
	ds_write_b128 v181, v[232:235] offset:16896
	s_waitcnt vmcnt(0)
	ds_write_b128 v181, v[236:239] offset:25344
	s_waitcnt lgkmcnt(0)
	s_barrier
	global_load_dwordx4 v[4:7], v[174:175], off
	global_load_dwordx4 v[140:143], v[174:175], off offset:32
	global_load_dwordx4 v[136:139], v[174:175], off offset:64
	global_load_dwordx4 v[132:135], v[174:175], off offset:96
	ds_read_b128 v[8:11], v177
	ds_read_b128 v[12:15], v177 offset:32
	s_waitcnt vmcnt(3) lgkmcnt(1)
	v_mfma_f32_32x32x16_bf16 v[116:131], v[8:11], v[4:7], 0
	ds_read_b128 v[8:11], v177 offset:64
	s_waitcnt vmcnt(2) lgkmcnt(1)
	v_mfma_f32_32x32x16_bf16 v[116:131], v[12:15], v[140:143], v[116:131]
	s_waitcnt vmcnt(1) lgkmcnt(0)
	v_mfma_f32_32x32x16_bf16 v[116:131], v[8:11], v[136:139], v[116:131]
	ds_read_b128 v[8:11], v177 offset:96
	s_waitcnt vmcnt(0) lgkmcnt(0)
	v_mfma_f32_32x32x16_bf16 v[116:131], v[8:11], v[132:135], v[116:131]
	ds_read_b128 v[8:11], v177 offset:16896
	s_waitcnt lgkmcnt(0)
	v_mfma_f32_32x32x16_bf16 v[100:115], v[8:11], v[4:7], 0
	ds_read_b128 v[8:11], v177 offset:16928
	s_waitcnt lgkmcnt(0)
	v_mfma_f32_32x32x16_bf16 v[100:115], v[8:11], v[140:143], v[100:115]
	ds_read_b128 v[8:11], v177 offset:16960
	s_waitcnt lgkmcnt(0)
	v_mfma_f32_32x32x16_bf16 v[100:115], v[8:11], v[136:139], v[100:115]
	ds_read_b128 v[8:11], v177 offset:16992
	s_waitcnt lgkmcnt(0)
	v_mfma_f32_32x32x16_bf16 v[100:115], v[8:11], v[132:135], v[100:115]
	ds_read_b128 v[8:11], v177 offset:33792
	s_waitcnt lgkmcnt(0)
	v_mfma_f32_32x32x16_bf16 v[84:99], v[8:11], v[4:7], 0
	ds_read_b128 v[8:11], v177 offset:33824
	s_waitcnt lgkmcnt(0)
	v_mfma_f32_32x32x16_bf16 v[84:99], v[8:11], v[140:143], v[84:99]
	ds_read_b128 v[8:11], v177 offset:33856
	s_waitcnt lgkmcnt(0)
	v_mfma_f32_32x32x16_bf16 v[84:99], v[8:11], v[136:139], v[84:99]
	ds_read_b128 v[8:11], v177 offset:33888
	s_waitcnt lgkmcnt(0)
	v_mfma_f32_32x32x16_bf16 v[84:99], v[8:11], v[132:135], v[84:99]
	ds_read_b128 v[8:11], v177 offset:50688
	s_waitcnt lgkmcnt(0)
	v_mfma_f32_32x32x16_bf16 v[68:83], v[8:11], v[4:7], 0
	ds_read_b128 v[8:11], v177 offset:50720
	s_waitcnt lgkmcnt(0)
	v_mfma_f32_32x32x16_bf16 v[68:83], v[8:11], v[140:143], v[68:83]
	ds_read_b128 v[8:11], v177 offset:50752
	s_waitcnt lgkmcnt(0)
	v_mfma_f32_32x32x16_bf16 v[68:83], v[8:11], v[136:139], v[68:83]
	ds_read_b128 v[8:11], v177 offset:50784
	s_waitcnt lgkmcnt(0)
	v_mfma_f32_32x32x16_bf16 v[68:83], v[8:11], v[132:135], v[68:83]
	ds_read_b128 v[8:11], v182
	ds_read_b128 v[12:15], v182 offset:32
	s_waitcnt lgkmcnt(1)
	v_mfma_f32_32x32x16_bf16 v[52:67], v[8:11], v[4:7], 0
	ds_read_b128 v[8:11], v182 offset:64
	s_waitcnt lgkmcnt(1)
	v_mfma_f32_32x32x16_bf16 v[52:67], v[12:15], v[140:143], v[52:67]
	s_waitcnt lgkmcnt(0)
	v_mfma_f32_32x32x16_bf16 v[52:67], v[8:11], v[136:139], v[52:67]
	ds_read_b128 v[8:11], v182 offset:96
	s_waitcnt lgkmcnt(0)
	v_mfma_f32_32x32x16_bf16 v[52:67], v[8:11], v[132:135], v[52:67]
	ds_read_b128 v[8:11], v183
	s_waitcnt lgkmcnt(0)
	v_mfma_f32_32x32x16_bf16 v[36:51], v[8:11], v[4:7], 0
	ds_read_b128 v[8:11], v183 offset:32
	s_waitcnt lgkmcnt(0)
	v_mfma_f32_32x32x16_bf16 v[36:51], v[8:11], v[140:143], v[36:51]
	ds_read_b128 v[8:11], v183 offset:64
	s_waitcnt lgkmcnt(0)
	v_mfma_f32_32x32x16_bf16 v[36:51], v[8:11], v[136:139], v[36:51]
	ds_read_b128 v[8:11], v183 offset:96
	s_waitcnt lgkmcnt(0)
	v_mfma_f32_32x32x16_bf16 v[36:51], v[8:11], v[132:135], v[36:51]
	ds_read_b128 v[8:11], v184
	ds_read_b128 v[12:15], v184 offset:32
	ds_read_b128 v[144:147], v185 offset:32
	s_waitcnt lgkmcnt(2)
	v_mfma_f32_32x32x16_bf16 v[20:35], v[8:11], v[4:7], 0
	ds_read_b128 v[8:11], v184 offset:64
	s_waitcnt lgkmcnt(2)
	v_mfma_f32_32x32x16_bf16 v[20:35], v[12:15], v[140:143], v[20:35]
	s_waitcnt lgkmcnt(0)
	v_mfma_f32_32x32x16_bf16 v[20:35], v[8:11], v[136:139], v[20:35]
	ds_read_b128 v[8:11], v184 offset:96
	s_waitcnt lgkmcnt(0)
	v_mfma_f32_32x32x16_bf16 v[20:35], v[8:11], v[132:135], v[20:35]
	ds_read_b128 v[8:11], v185
	s_waitcnt lgkmcnt(0)
	v_mfma_f32_32x32x16_bf16 v[4:19], v[8:11], v[4:7], 0
	v_mfma_f32_32x32x16_bf16 v[4:19], v[144:147], v[140:143], v[4:19]
	ds_read_b128 v[140:143], v185 offset:64
	s_waitcnt lgkmcnt(0)
	v_mfma_f32_32x32x16_bf16 v[4:19], v[140:143], v[136:139], v[4:19]
	ds_read_b128 v[136:139], v185 offset:96
	s_waitcnt lgkmcnt(0)
	v_mfma_f32_32x32x16_bf16 v[4:19], v[136:139], v[132:135], v[4:19]
	global_load_dwordx4 v[132:135], v[174:175], off offset:128
	global_load_dwordx4 v[136:139], v[174:175], off offset:160
	global_load_dwordx4 v[140:143], v[174:175], off offset:192
	global_load_dwordx4 v[144:147], v[174:175], off offset:224
	ds_read_b128 v[188:191], v177 offset:128
	s_waitcnt vmcnt(3) lgkmcnt(0)
	v_mfma_f32_32x32x16_bf16 v[116:131], v[188:191], v[132:135], v[116:131]
	ds_read_b128 v[188:191], v177 offset:160
	s_waitcnt vmcnt(2) lgkmcnt(0)
	v_mfma_f32_32x32x16_bf16 v[116:131], v[188:191], v[136:139], v[116:131]
	ds_read_b128 v[188:191], v177 offset:192
	s_waitcnt vmcnt(1) lgkmcnt(0)
	v_mfma_f32_32x32x16_bf16 v[116:131], v[188:191], v[140:143], v[116:131]
	ds_read_b128 v[188:191], v177 offset:224
	s_waitcnt vmcnt(0) lgkmcnt(0)
	v_mfma_f32_32x32x16_bf16 v[116:131], v[188:191], v[144:147], v[116:131]
	ds_read_b128 v[188:191], v177 offset:17024
	s_waitcnt lgkmcnt(0)
	v_mfma_f32_32x32x16_bf16 v[100:115], v[188:191], v[132:135], v[100:115]
	ds_read_b128 v[188:191], v177 offset:17056
	s_waitcnt lgkmcnt(0)
	v_mfma_f32_32x32x16_bf16 v[100:115], v[188:191], v[136:139], v[100:115]
	ds_read_b128 v[188:191], v177 offset:17088
	s_waitcnt lgkmcnt(0)
	v_mfma_f32_32x32x16_bf16 v[100:115], v[188:191], v[140:143], v[100:115]
	ds_read_b128 v[188:191], v177 offset:17120
	s_waitcnt lgkmcnt(0)
	v_mfma_f32_32x32x16_bf16 v[100:115], v[188:191], v[144:147], v[100:115]
	ds_read_b128 v[188:191], v177 offset:33920
	s_waitcnt lgkmcnt(0)
	v_mfma_f32_32x32x16_bf16 v[84:99], v[188:191], v[132:135], v[84:99]
	ds_read_b128 v[188:191], v177 offset:33952
	s_waitcnt lgkmcnt(0)
	v_mfma_f32_32x32x16_bf16 v[84:99], v[188:191], v[136:139], v[84:99]
	ds_read_b128 v[188:191], v177 offset:33984
	s_waitcnt lgkmcnt(0)
	v_mfma_f32_32x32x16_bf16 v[84:99], v[188:191], v[140:143], v[84:99]
	ds_read_b128 v[188:191], v177 offset:34016
	s_waitcnt lgkmcnt(0)
	v_mfma_f32_32x32x16_bf16 v[84:99], v[188:191], v[144:147], v[84:99]
	ds_read_b128 v[188:191], v177 offset:50816
	s_waitcnt lgkmcnt(0)
	v_mfma_f32_32x32x16_bf16 v[68:83], v[188:191], v[132:135], v[68:83]
	ds_read_b128 v[188:191], v177 offset:50848
	s_waitcnt lgkmcnt(0)
	v_mfma_f32_32x32x16_bf16 v[68:83], v[188:191], v[136:139], v[68:83]
	ds_read_b128 v[188:191], v177 offset:50880
	s_waitcnt lgkmcnt(0)
	v_mfma_f32_32x32x16_bf16 v[68:83], v[188:191], v[140:143], v[68:83]
	ds_read_b128 v[188:191], v177 offset:50912
	s_waitcnt lgkmcnt(0)
	v_mfma_f32_32x32x16_bf16 v[68:83], v[188:191], v[144:147], v[68:83]
	ds_read_b128 v[188:191], v182 offset:128
	s_waitcnt lgkmcnt(0)
	v_mfma_f32_32x32x16_bf16 v[52:67], v[188:191], v[132:135], v[52:67]
	ds_read_b128 v[188:191], v182 offset:160
	s_waitcnt lgkmcnt(0)
	v_mfma_f32_32x32x16_bf16 v[52:67], v[188:191], v[136:139], v[52:67]
	ds_read_b128 v[188:191], v182 offset:192
	s_waitcnt lgkmcnt(0)
	v_mfma_f32_32x32x16_bf16 v[52:67], v[188:191], v[140:143], v[52:67]
	ds_read_b128 v[188:191], v182 offset:224
	s_waitcnt lgkmcnt(0)
	v_mfma_f32_32x32x16_bf16 v[52:67], v[188:191], v[144:147], v[52:67]
	ds_read_b128 v[188:191], v186 offset:128
	ds_read_b128 v[192:195], v186 offset:160
	s_waitcnt lgkmcnt(1)
	v_mfma_f32_32x32x16_bf16 v[36:51], v[188:191], v[132:135], v[36:51]
	ds_read_b128 v[188:191], v186 offset:192
	s_waitcnt lgkmcnt(1)
	v_mfma_f32_32x32x16_bf16 v[36:51], v[192:195], v[136:139], v[36:51]
	s_waitcnt lgkmcnt(0)
	v_mfma_f32_32x32x16_bf16 v[36:51], v[188:191], v[140:143], v[36:51]
	ds_read_b128 v[188:191], v186 offset:224
	s_waitcnt lgkmcnt(0)
	v_mfma_f32_32x32x16_bf16 v[36:51], v[188:191], v[144:147], v[36:51]
	ds_read_b128 v[188:191], v184 offset:128
	s_waitcnt lgkmcnt(0)
	v_mfma_f32_32x32x16_bf16 v[20:35], v[188:191], v[132:135], v[20:35]
	ds_read_b128 v[188:191], v184 offset:160
	s_waitcnt lgkmcnt(0)
	v_mfma_f32_32x32x16_bf16 v[20:35], v[188:191], v[136:139], v[20:35]
	ds_read_b128 v[188:191], v184 offset:192
	s_waitcnt lgkmcnt(0)
	v_mfma_f32_32x32x16_bf16 v[20:35], v[188:191], v[140:143], v[20:35]
	ds_read_b128 v[188:191], v184 offset:224
	s_waitcnt lgkmcnt(0)
	v_mfma_f32_32x32x16_bf16 v[20:35], v[188:191], v[144:147], v[20:35]
	ds_read_b128 v[188:191], v187 offset:128
	ds_read_b128 v[192:195], v187 offset:160
	s_waitcnt lgkmcnt(1)
	v_mfma_f32_32x32x16_bf16 v[4:19], v[188:191], v[132:135], v[4:19]
	ds_read_b128 v[132:135], v187 offset:192
	s_waitcnt lgkmcnt(1)
	v_mfma_f32_32x32x16_bf16 v[4:19], v[192:195], v[136:139], v[4:19]
	s_waitcnt lgkmcnt(0)
	v_mfma_f32_32x32x16_bf16 v[4:19], v[132:135], v[140:143], v[4:19]
	ds_read_b128 v[132:135], v187 offset:224
	s_waitcnt lgkmcnt(0)
	v_mfma_f32_32x32x16_bf16 v[4:19], v[132:135], v[144:147], v[4:19]
	global_load_dwordx4 v[132:135], v[174:175], off offset:256
	global_load_dwordx4 v[136:139], v[174:175], off offset:288
	global_load_dwordx4 v[140:143], v[174:175], off offset:320
	global_load_dwordx4 v[144:147], v[174:175], off offset:352
	ds_read_b128 v[188:191], v177 offset:256
	s_waitcnt vmcnt(3) lgkmcnt(0)
	v_mfma_f32_32x32x16_bf16 v[116:131], v[188:191], v[132:135], v[116:131]
	ds_read_b128 v[188:191], v177 offset:288
	s_waitcnt vmcnt(2) lgkmcnt(0)
	v_mfma_f32_32x32x16_bf16 v[116:131], v[188:191], v[136:139], v[116:131]
	ds_read_b128 v[188:191], v177 offset:320
	s_waitcnt vmcnt(1) lgkmcnt(0)
	v_mfma_f32_32x32x16_bf16 v[116:131], v[188:191], v[140:143], v[116:131]
	ds_read_b128 v[188:191], v177 offset:352
	s_waitcnt vmcnt(0) lgkmcnt(0)
	v_mfma_f32_32x32x16_bf16 v[116:131], v[188:191], v[144:147], v[116:131]
	ds_read_b128 v[188:191], v177 offset:17152
	s_waitcnt lgkmcnt(0)
	v_mfma_f32_32x32x16_bf16 v[100:115], v[188:191], v[132:135], v[100:115]
	ds_read_b128 v[188:191], v177 offset:17184
	s_waitcnt lgkmcnt(0)
	v_mfma_f32_32x32x16_bf16 v[100:115], v[188:191], v[136:139], v[100:115]
	ds_read_b128 v[188:191], v177 offset:17216
	s_waitcnt lgkmcnt(0)
	v_mfma_f32_32x32x16_bf16 v[100:115], v[188:191], v[140:143], v[100:115]
	ds_read_b128 v[188:191], v177 offset:17248
	s_waitcnt lgkmcnt(0)
	v_mfma_f32_32x32x16_bf16 v[100:115], v[188:191], v[144:147], v[100:115]
	ds_read_b128 v[188:191], v177 offset:34048
	s_waitcnt lgkmcnt(0)
	v_mfma_f32_32x32x16_bf16 v[84:99], v[188:191], v[132:135], v[84:99]
	ds_read_b128 v[188:191], v177 offset:34080
	s_waitcnt lgkmcnt(0)
	v_mfma_f32_32x32x16_bf16 v[84:99], v[188:191], v[136:139], v[84:99]
	ds_read_b128 v[188:191], v177 offset:34112
	s_waitcnt lgkmcnt(0)
	v_mfma_f32_32x32x16_bf16 v[84:99], v[188:191], v[140:143], v[84:99]
	ds_read_b128 v[188:191], v177 offset:34144
	s_waitcnt lgkmcnt(0)
	v_mfma_f32_32x32x16_bf16 v[84:99], v[188:191], v[144:147], v[84:99]
	ds_read_b128 v[188:191], v177 offset:50944
	s_waitcnt lgkmcnt(0)
	v_mfma_f32_32x32x16_bf16 v[68:83], v[188:191], v[132:135], v[68:83]
	ds_read_b128 v[188:191], v177 offset:50976
	s_waitcnt lgkmcnt(0)
	v_mfma_f32_32x32x16_bf16 v[68:83], v[188:191], v[136:139], v[68:83]
	ds_read_b128 v[188:191], v177 offset:51008
	s_waitcnt lgkmcnt(0)
	v_mfma_f32_32x32x16_bf16 v[68:83], v[188:191], v[140:143], v[68:83]
	ds_read_b128 v[188:191], v177 offset:51040
	s_waitcnt lgkmcnt(0)
	v_mfma_f32_32x32x16_bf16 v[68:83], v[188:191], v[144:147], v[68:83]
	ds_read_b128 v[188:191], v182 offset:256
	s_waitcnt lgkmcnt(0)
	v_mfma_f32_32x32x16_bf16 v[52:67], v[188:191], v[132:135], v[52:67]
	ds_read_b128 v[188:191], v182 offset:288
	s_waitcnt lgkmcnt(0)
	v_mfma_f32_32x32x16_bf16 v[52:67], v[188:191], v[136:139], v[52:67]
	ds_read_b128 v[188:191], v182 offset:320
	s_waitcnt lgkmcnt(0)
	v_mfma_f32_32x32x16_bf16 v[52:67], v[188:191], v[140:143], v[52:67]
	ds_read_b128 v[188:191], v182 offset:352
	s_waitcnt lgkmcnt(0)
	v_mfma_f32_32x32x16_bf16 v[52:67], v[188:191], v[144:147], v[52:67]
	ds_read_b128 v[188:191], v186 offset:256
	s_waitcnt lgkmcnt(0)
	v_mfma_f32_32x32x16_bf16 v[36:51], v[188:191], v[132:135], v[36:51]
	ds_read_b128 v[188:191], v186 offset:288
	s_waitcnt lgkmcnt(0)
	v_mfma_f32_32x32x16_bf16 v[36:51], v[188:191], v[136:139], v[36:51]
	ds_read_b128 v[188:191], v186 offset:320
	s_waitcnt lgkmcnt(0)
	v_mfma_f32_32x32x16_bf16 v[36:51], v[188:191], v[140:143], v[36:51]
	ds_read_b128 v[188:191], v186 offset:352
	s_waitcnt lgkmcnt(0)
	v_mfma_f32_32x32x16_bf16 v[36:51], v[188:191], v[144:147], v[36:51]
	ds_read_b128 v[188:191], v184 offset:256
	s_waitcnt lgkmcnt(0)
	v_mfma_f32_32x32x16_bf16 v[20:35], v[188:191], v[132:135], v[20:35]
	ds_read_b128 v[188:191], v184 offset:288
	s_waitcnt lgkmcnt(0)
	v_mfma_f32_32x32x16_bf16 v[20:35], v[188:191], v[136:139], v[20:35]
	ds_read_b128 v[188:191], v184 offset:320
	s_waitcnt lgkmcnt(0)
	v_mfma_f32_32x32x16_bf16 v[20:35], v[188:191], v[140:143], v[20:35]
	ds_read_b128 v[188:191], v184 offset:352
	s_waitcnt lgkmcnt(0)
	v_mfma_f32_32x32x16_bf16 v[20:35], v[188:191], v[144:147], v[20:35]
	ds_read_b128 v[188:191], v187 offset:256
	s_waitcnt lgkmcnt(0)
	v_mfma_f32_32x32x16_bf16 v[4:19], v[188:191], v[132:135], v[4:19]
	ds_read_b128 v[132:135], v187 offset:288
	s_waitcnt lgkmcnt(0)
	v_mfma_f32_32x32x16_bf16 v[4:19], v[132:135], v[136:139], v[4:19]
	ds_read_b128 v[132:135], v187 offset:320
	s_waitcnt lgkmcnt(0)
	v_mfma_f32_32x32x16_bf16 v[4:19], v[132:135], v[140:143], v[4:19]
	ds_read_b128 v[132:135], v187 offset:352
	s_waitcnt lgkmcnt(0)
	v_mfma_f32_32x32x16_bf16 v[4:19], v[132:135], v[144:147], v[4:19]
	global_load_dwordx4 v[136:139], v[174:175], off offset:384
	global_load_dwordx4 v[144:147], v[174:175], off offset:416
	global_load_dwordx4 v[140:143], v[174:175], off offset:448
	global_load_dwordx4 v[132:135], v[174:175], off offset:480
	ds_read_b128 v[188:191], v177 offset:384
	s_waitcnt vmcnt(3) lgkmcnt(0)
	v_mfma_f32_32x32x16_bf16 v[116:131], v[188:191], v[136:139], v[116:131]
	ds_read_b128 v[188:191], v177 offset:416
	s_waitcnt vmcnt(2) lgkmcnt(0)
	v_mfma_f32_32x32x16_bf16 v[116:131], v[188:191], v[144:147], v[116:131]
	ds_read_b128 v[188:191], v177 offset:448
	s_waitcnt vmcnt(1) lgkmcnt(0)
	v_mfma_f32_32x32x16_bf16 v[116:131], v[188:191], v[140:143], v[116:131]
	ds_read_b128 v[188:191], v177 offset:480
	s_waitcnt vmcnt(0) lgkmcnt(0)
	v_mfma_f32_32x32x16_bf16 v[116:131], v[188:191], v[132:135], v[116:131]
	ds_read_b128 v[188:191], v177 offset:17280
	s_waitcnt lgkmcnt(0)
	v_mfma_f32_32x32x16_bf16 v[100:115], v[188:191], v[136:139], v[100:115]
	ds_read_b128 v[188:191], v177 offset:17312
	s_waitcnt lgkmcnt(0)
	v_mfma_f32_32x32x16_bf16 v[100:115], v[188:191], v[144:147], v[100:115]
	ds_read_b128 v[188:191], v177 offset:17344
	s_waitcnt lgkmcnt(0)
	v_mfma_f32_32x32x16_bf16 v[100:115], v[188:191], v[140:143], v[100:115]
	ds_read_b128 v[188:191], v177 offset:17376
	s_waitcnt lgkmcnt(0)
	v_mfma_f32_32x32x16_bf16 v[100:115], v[188:191], v[132:135], v[100:115]
	ds_read_b128 v[188:191], v177 offset:34176
	s_waitcnt lgkmcnt(0)
	v_mfma_f32_32x32x16_bf16 v[84:99], v[188:191], v[136:139], v[84:99]
	ds_read_b128 v[188:191], v177 offset:34208
	s_waitcnt lgkmcnt(0)
	v_mfma_f32_32x32x16_bf16 v[84:99], v[188:191], v[144:147], v[84:99]
	ds_read_b128 v[188:191], v177 offset:34240
	s_waitcnt lgkmcnt(0)
	v_mfma_f32_32x32x16_bf16 v[84:99], v[188:191], v[140:143], v[84:99]
	ds_read_b128 v[188:191], v177 offset:34272
	s_waitcnt lgkmcnt(0)
	v_mfma_f32_32x32x16_bf16 v[84:99], v[188:191], v[132:135], v[84:99]
	ds_read_b128 v[188:191], v177 offset:51072
	s_waitcnt lgkmcnt(0)
	v_mfma_f32_32x32x16_bf16 v[68:83], v[188:191], v[136:139], v[68:83]
	ds_read_b128 v[188:191], v177 offset:51104
	s_waitcnt lgkmcnt(0)
	v_mfma_f32_32x32x16_bf16 v[68:83], v[188:191], v[144:147], v[68:83]
	ds_read_b128 v[188:191], v177 offset:51136
	s_waitcnt lgkmcnt(0)
	v_mfma_f32_32x32x16_bf16 v[68:83], v[188:191], v[140:143], v[68:83]
	ds_read_b128 v[188:191], v177 offset:51168
	s_waitcnt lgkmcnt(0)
	v_mfma_f32_32x32x16_bf16 v[68:83], v[188:191], v[132:135], v[68:83]
	ds_read_b128 v[188:191], v182 offset:384
	s_waitcnt lgkmcnt(0)
	v_mfma_f32_32x32x16_bf16 v[52:67], v[188:191], v[136:139], v[52:67]
	ds_read_b128 v[188:191], v182 offset:416
	s_waitcnt lgkmcnt(0)
	v_mfma_f32_32x32x16_bf16 v[52:67], v[188:191], v[144:147], v[52:67]
	ds_read_b128 v[188:191], v182 offset:448
	s_waitcnt lgkmcnt(0)
	v_mfma_f32_32x32x16_bf16 v[52:67], v[188:191], v[140:143], v[52:67]
	ds_read_b128 v[188:191], v182 offset:480
	s_waitcnt lgkmcnt(0)
	v_mfma_f32_32x32x16_bf16 v[52:67], v[188:191], v[132:135], v[52:67]
	ds_read_b128 v[188:191], v186 offset:384
	s_waitcnt lgkmcnt(0)
	v_mfma_f32_32x32x16_bf16 v[36:51], v[188:191], v[136:139], v[36:51]
	ds_read_b128 v[188:191], v186 offset:416
	s_waitcnt lgkmcnt(0)
	v_mfma_f32_32x32x16_bf16 v[36:51], v[188:191], v[144:147], v[36:51]
	ds_read_b128 v[188:191], v186 offset:448
	s_waitcnt lgkmcnt(0)
	v_mfma_f32_32x32x16_bf16 v[36:51], v[188:191], v[140:143], v[36:51]
	ds_read_b128 v[188:191], v186 offset:480
	s_waitcnt lgkmcnt(0)
	v_mfma_f32_32x32x16_bf16 v[36:51], v[188:191], v[132:135], v[36:51]
	ds_read_b128 v[188:191], v184 offset:384
	s_waitcnt lgkmcnt(0)
	v_mfma_f32_32x32x16_bf16 v[20:35], v[188:191], v[136:139], v[20:35]
	ds_read_b128 v[188:191], v184 offset:416
	s_waitcnt lgkmcnt(0)
	v_mfma_f32_32x32x16_bf16 v[20:35], v[188:191], v[144:147], v[20:35]
	ds_read_b128 v[188:191], v184 offset:448
	s_waitcnt lgkmcnt(0)
	v_mfma_f32_32x32x16_bf16 v[20:35], v[188:191], v[140:143], v[20:35]
	ds_read_b128 v[188:191], v184 offset:480
	s_waitcnt lgkmcnt(0)
	v_mfma_f32_32x32x16_bf16 v[20:35], v[188:191], v[132:135], v[20:35]
	ds_read_b128 v[188:191], v187 offset:384
	s_waitcnt lgkmcnt(0)
	v_mfma_f32_32x32x16_bf16 v[4:19], v[188:191], v[136:139], v[4:19]
	ds_read_b128 v[136:139], v187 offset:416
	s_waitcnt lgkmcnt(0)
	v_mfma_f32_32x32x16_bf16 v[4:19], v[136:139], v[144:147], v[4:19]
	ds_read_b128 v[136:139], v187 offset:448
	s_waitcnt lgkmcnt(0)
	v_mfma_f32_32x32x16_bf16 v[4:19], v[136:139], v[140:143], v[4:19]
	ds_read_b128 v[136:139], v187 offset:480
	s_waitcnt lgkmcnt(0)
	s_barrier
	v_mfma_f32_32x32x16_bf16 v[4:19], v[136:139], v[132:135], v[4:19]
	v_max_f32_e32 v132, v117, v117
	v_max_f32_e32 v133, v116, v116
	v_max_f32_e32 v132, v133, v132
	v_max3_f32 v132, v132, v118, v119
	v_max3_f32 v132, v132, v120, v121
	v_max3_f32 v132, v132, v122, v123
	v_max3_f32 v132, v132, v124, v125
	v_max3_f32 v132, v132, v126, v127
	v_max3_f32 v132, v132, v128, v129
	v_max3_f32 v132, v132, v130, v131
	v_max3_f32 v132, v132, v100, v101
	v_max3_f32 v132, v132, v102, v103
	v_max3_f32 v132, v132, v104, v105
	v_max3_f32 v132, v132, v106, v107
	v_max3_f32 v132, v132, v108, v109
	v_max3_f32 v132, v132, v110, v111
	v_max3_f32 v132, v132, v112, v113
	v_max3_f32 v132, v132, v114, v115
	v_max3_f32 v132, v132, v84, v85
	v_max3_f32 v132, v132, v86, v87
	v_max3_f32 v132, v132, v88, v89
	v_max3_f32 v132, v132, v90, v91
	v_max3_f32 v132, v132, v92, v93
	v_max3_f32 v132, v132, v94, v95
	v_max3_f32 v132, v132, v96, v97
	v_max3_f32 v132, v132, v98, v99
	v_max3_f32 v132, v132, v68, v69
	v_max3_f32 v132, v132, v70, v71
	v_max3_f32 v132, v132, v72, v73
	v_max3_f32 v132, v132, v74, v75
	v_max3_f32 v132, v132, v76, v77
	v_max3_f32 v132, v132, v78, v79
	v_max3_f32 v132, v132, v80, v81
	v_max3_f32 v132, v132, v82, v83
	v_max3_f32 v132, v132, v52, v53
	v_max3_f32 v132, v132, v54, v55
	v_max3_f32 v132, v132, v56, v57
	v_max3_f32 v132, v132, v58, v59
	v_max3_f32 v132, v132, v60, v61
	v_max3_f32 v132, v132, v62, v63
	v_max3_f32 v132, v132, v64, v65
	v_max3_f32 v132, v132, v66, v67
	v_max3_f32 v132, v132, v36, v37
	v_max3_f32 v132, v132, v38, v39
	v_max3_f32 v132, v132, v40, v41
	v_max3_f32 v132, v132, v42, v43
	v_max3_f32 v132, v132, v44, v45
	v_max3_f32 v132, v132, v46, v47
	v_max3_f32 v132, v132, v48, v49
	v_max3_f32 v132, v132, v50, v51
	v_max3_f32 v132, v132, v20, v21
	v_max3_f32 v132, v132, v22, v23
	v_max3_f32 v132, v132, v24, v25
	v_max3_f32 v132, v132, v26, v27
	v_max3_f32 v132, v132, v28, v29
	v_max3_f32 v132, v132, v30, v31
	v_max3_f32 v132, v132, v32, v33
	v_max3_f32 v132, v132, v34, v35
	v_max3_f32 v132, v132, v4, v5
	v_max3_f32 v132, v132, v6, v7
	v_max3_f32 v132, v132, v8, v9
	v_max3_f32 v132, v132, v10, v11
	v_and_b32_e32 v134, 64, v250
	v_max3_f32 v132, v132, v12, v13
	v_xor_b32_e32 v133, 32, v250
	v_add_u32_e32 v134, 64, v134
	v_max3_f32 v132, v132, v14, v15
	v_cmp_lt_i32_e32 vcc, v133, v134
	v_max3_f32 v132, v132, v16, v17
	v_max3_f32 v132, v132, v18, v19
	v_cndmask_b32_e32 v133, v250, v133, vcc
	v_lshlrev_b32_e32 v134, 2, v133
	ds_bpermute_b32 v133, v134, v132
	s_waitcnt lgkmcnt(0)
	v_max_f32_e32 v133, v133, v133
	v_max_f32_e32 v133, v132, v133
	v_mov_b32_e32 v132, v19
	v_pk_mul_f32 v[132:133], v[172:173], v[132:133] op_sel_hi:[0,1]
	v_fma_f32 v19, v172, v116, -v133
	v_exp_f32_e32 v19, v19
	v_fma_f32 v116, v172, v117, -v133
	v_exp_f32_e32 v116, v116
	v_fma_f32 v117, v172, v118, -v133
	v_exp_f32_e32 v117, v117
	v_fma_f32 v118, v172, v119, -v133
	v_exp_f32_e32 v118, v118
	v_fma_f32 v119, v172, v120, -v133
	v_add_f32_e32 v135, 0, v19
	v_exp_f32_e32 v119, v119
	v_fma_f32 v120, v172, v121, -v133
	v_add_f32_e32 v135, v116, v135
	v_exp_f32_e32 v120, v120
	v_fma_f32 v121, v172, v122, -v133
	v_add_f32_e32 v135, v117, v135
	v_exp_f32_e32 v121, v121
	v_fma_f32 v122, v172, v123, -v133
	v_add_f32_e32 v135, v118, v135
	v_exp_f32_e32 v122, v122
	v_fma_f32 v123, v172, v124, -v133
	v_add_f32_e32 v135, v119, v135
	v_exp_f32_e32 v123, v123
	v_fma_f32 v124, v172, v125, -v133
	v_add_f32_e32 v135, v120, v135
	v_exp_f32_e32 v124, v124
	v_fma_f32 v125, v172, v126, -v133
	v_add_f32_e32 v135, v121, v135
	v_exp_f32_e32 v125, v125
	v_fma_f32 v126, v172, v127, -v133
	v_add_f32_e32 v135, v122, v135
	v_exp_f32_e32 v126, v126
	v_fma_f32 v127, v172, v128, -v133
	v_add_f32_e32 v135, v123, v135
	v_exp_f32_e32 v127, v127
	v_fma_f32 v128, v172, v129, -v133
	v_add_f32_e32 v135, v124, v135
	v_exp_f32_e32 v128, v128
	v_fma_f32 v129, v172, v130, -v133
	v_add_f32_e32 v135, v125, v135
	v_exp_f32_e32 v129, v129
	v_fma_f32 v130, v172, v131, -v133
	v_add_f32_e32 v135, v126, v135
	v_exp_f32_e32 v130, v130
	v_fma_f32 v100, v172, v100, -v133
	v_add_f32_e32 v135, v127, v135
	v_exp_f32_e32 v100, v100
	v_fma_f32 v101, v172, v101, -v133
	v_add_f32_e32 v135, v128, v135
	v_exp_f32_e32 v101, v101
	v_fma_f32 v102, v172, v102, -v133
	v_add_f32_e32 v135, v129, v135
	v_exp_f32_e32 v102, v102
	v_fma_f32 v103, v172, v103, -v133
	v_add_f32_e32 v131, v130, v135
	v_exp_f32_e32 v103, v103
	v_fma_f32 v104, v172, v104, -v133
	v_add_f32_e32 v131, v100, v131
	v_exp_f32_e32 v104, v104
	v_fma_f32 v105, v172, v105, -v133
	v_add_f32_e32 v131, v101, v131
	v_exp_f32_e32 v105, v105
	v_fma_f32 v106, v172, v106, -v133
	v_add_f32_e32 v131, v102, v131
	v_exp_f32_e32 v106, v106
	v_fma_f32 v107, v172, v107, -v133
	v_add_f32_e32 v131, v103, v131
	v_exp_f32_e32 v107, v107
	v_fma_f32 v108, v172, v108, -v133
	v_add_f32_e32 v131, v104, v131
	v_exp_f32_e32 v108, v108
	v_fma_f32 v109, v172, v109, -v133
	v_add_f32_e32 v131, v105, v131
	v_exp_f32_e32 v109, v109
	v_fma_f32 v110, v172, v110, -v133
	v_add_f32_e32 v131, v106, v131
	v_exp_f32_e32 v110, v110
	v_fma_f32 v111, v172, v111, -v133
	v_add_f32_e32 v131, v107, v131
	v_exp_f32_e32 v111, v111
	v_fma_f32 v112, v172, v112, -v133
	v_add_f32_e32 v131, v108, v131
	v_exp_f32_e32 v112, v112
	v_fma_f32 v113, v172, v113, -v133
	v_add_f32_e32 v131, v109, v131
	v_exp_f32_e32 v113, v113
	v_fma_f32 v114, v172, v114, -v133
	v_add_f32_e32 v131, v110, v131
	v_exp_f32_e32 v114, v114
	v_fma_f32 v115, v172, v115, -v133
	v_add_f32_e32 v131, v111, v131
	v_exp_f32_e32 v115, v115
	v_fma_f32 v84, v172, v84, -v133
	v_add_f32_e32 v131, v112, v131
	v_exp_f32_e32 v84, v84
	v_fma_f32 v85, v172, v85, -v133
	v_add_f32_e32 v131, v113, v131
	v_exp_f32_e32 v85, v85
	v_fma_f32 v86, v172, v86, -v133
	v_add_f32_e32 v131, v114, v131
	v_exp_f32_e32 v86, v86
	v_fma_f32 v87, v172, v87, -v133
	v_add_f32_e32 v131, v115, v131
	v_exp_f32_e32 v87, v87
	v_fma_f32 v88, v172, v88, -v133
	v_add_f32_e32 v131, v84, v131
	v_exp_f32_e32 v88, v88
	v_fma_f32 v89, v172, v89, -v133
	v_add_f32_e32 v131, v85, v131
	v_exp_f32_e32 v89, v89
	v_fma_f32 v90, v172, v90, -v133
	v_add_f32_e32 v131, v86, v131
	v_exp_f32_e32 v90, v90
	v_fma_f32 v91, v172, v91, -v133
	v_add_f32_e32 v131, v87, v131
	v_exp_f32_e32 v91, v91
	v_fma_f32 v92, v172, v92, -v133
	v_add_f32_e32 v131, v88, v131
	v_exp_f32_e32 v92, v92
	v_fma_f32 v93, v172, v93, -v133
	v_add_f32_e32 v131, v89, v131
	v_exp_f32_e32 v93, v93
	v_fma_f32 v94, v172, v94, -v133
	v_add_f32_e32 v131, v90, v131
	v_exp_f32_e32 v94, v94
	v_fma_f32 v95, v172, v95, -v133
	v_add_f32_e32 v131, v91, v131
	v_exp_f32_e32 v95, v95
	v_fma_f32 v96, v172, v96, -v133
	v_add_f32_e32 v131, v92, v131
	v_exp_f32_e32 v96, v96
	v_fma_f32 v97, v172, v97, -v133
	v_add_f32_e32 v131, v93, v131
	v_exp_f32_e32 v97, v97
	v_fma_f32 v98, v172, v98, -v133
	v_add_f32_e32 v131, v94, v131
	v_exp_f32_e32 v98, v98
	v_fma_f32 v99, v172, v99, -v133
	v_add_f32_e32 v131, v95, v131
	v_exp_f32_e32 v99, v99
	v_fma_f32 v68, v172, v68, -v133
	v_add_f32_e32 v131, v96, v131
	v_exp_f32_e32 v68, v68
	v_fma_f32 v69, v172, v69, -v133
	v_add_f32_e32 v131, v97, v131
	v_exp_f32_e32 v69, v69
	v_fma_f32 v70, v172, v70, -v133
	v_add_f32_e32 v131, v98, v131
	v_exp_f32_e32 v70, v70
	v_fma_f32 v71, v172, v71, -v133
	v_add_f32_e32 v131, v99, v131
	v_exp_f32_e32 v71, v71
	v_fma_f32 v72, v172, v72, -v133
	v_add_f32_e32 v131, v68, v131
	v_exp_f32_e32 v72, v72
	v_fma_f32 v73, v172, v73, -v133
	v_add_f32_e32 v131, v69, v131
	v_exp_f32_e32 v73, v73
	v_fma_f32 v74, v172, v74, -v133
	v_add_f32_e32 v131, v70, v131
	v_exp_f32_e32 v74, v74
	v_fma_f32 v75, v172, v75, -v133
	v_add_f32_e32 v131, v71, v131
	v_exp_f32_e32 v75, v75
	v_fma_f32 v76, v172, v76, -v133
	v_add_f32_e32 v131, v72, v131
	v_exp_f32_e32 v76, v76
	v_fma_f32 v77, v172, v77, -v133
	v_add_f32_e32 v131, v73, v131
	v_exp_f32_e32 v77, v77
	v_fma_f32 v78, v172, v78, -v133
	v_add_f32_e32 v131, v74, v131
	v_exp_f32_e32 v78, v78
	v_fma_f32 v79, v172, v79, -v133
	v_add_f32_e32 v131, v75, v131
	v_exp_f32_e32 v79, v79
	v_fma_f32 v80, v172, v80, -v133
	v_add_f32_e32 v131, v76, v131
	v_exp_f32_e32 v80, v80
	v_fma_f32 v81, v172, v81, -v133
	v_add_f32_e32 v131, v77, v131
	v_exp_f32_e32 v81, v81
	v_fma_f32 v82, v172, v82, -v133
	v_add_f32_e32 v131, v78, v131
	v_exp_f32_e32 v82, v82
	v_fma_f32 v83, v172, v83, -v133
	v_add_f32_e32 v131, v79, v131
	v_exp_f32_e32 v83, v83
	v_fma_f32 v52, v172, v52, -v133
	v_add_f32_e32 v131, v80, v131
	v_exp_f32_e32 v135, v52
	v_fma_f32 v53, v172, v53, -v133
	v_add_f32_e32 v131, v81, v131
	v_exp_f32_e32 v136, v53
	v_fma_f32 v53, v172, v54, -v133
	v_add_f32_e32 v131, v82, v131
	v_exp_f32_e32 v137, v53
	v_fma_f32 v53, v172, v55, -v133
	v_add_f32_e32 v131, v83, v131
	v_exp_f32_e32 v138, v53
	v_fma_f32 v53, v172, v56, -v133
	v_add_f32_e32 v52, v135, v131
	v_exp_f32_e32 v139, v53
	v_fma_f32 v53, v172, v57, -v133
	v_add_f32_e32 v52, v136, v52
	v_exp_f32_e32 v140, v53
	v_fma_f32 v53, v172, v58, -v133
	v_add_f32_e32 v52, v137, v52
	v_exp_f32_e32 v141, v53
	v_fma_f32 v53, v172, v59, -v133
	v_add_f32_e32 v52, v138, v52
	v_exp_f32_e32 v142, v53
	v_fma_f32 v53, v172, v60, -v133
	v_add_f32_e32 v52, v139, v52
	v_exp_f32_e32 v143, v53
	v_fma_f32 v53, v172, v61, -v133
	v_add_f32_e32 v52, v140, v52
	v_exp_f32_e32 v144, v53
	v_fma_f32 v53, v172, v62, -v133
	v_add_f32_e32 v52, v141, v52
	v_exp_f32_e32 v145, v53
	v_fma_f32 v53, v172, v63, -v133
	v_add_f32_e32 v52, v142, v52
	v_exp_f32_e32 v146, v53
	v_fma_f32 v53, v172, v64, -v133
	v_add_f32_e32 v52, v143, v52
	v_exp_f32_e32 v147, v53
	v_fma_f32 v53, v172, v65, -v133
	v_add_f32_e32 v52, v144, v52
	v_exp_f32_e32 v174, v53
	v_fma_f32 v53, v172, v66, -v133
	v_add_f32_e32 v52, v145, v52
	v_exp_f32_e32 v175, v53
	v_fma_f32 v53, v172, v67, -v133
	v_add_f32_e32 v52, v146, v52
	v_exp_f32_e32 v188, v53
	v_fma_f32 v36, v172, v36, -v133
	v_add_f32_e32 v52, v147, v52
	v_exp_f32_e32 v189, v36
	v_fma_f32 v37, v172, v37, -v133
	v_add_f32_e32 v52, v174, v52
	v_exp_f32_e32 v190, v37
	v_fma_f32 v37, v172, v38, -v133
	v_add_f32_e32 v52, v175, v52
	v_exp_f32_e32 v191, v37
	v_fma_f32 v37, v172, v39, -v133
	v_add_f32_e32 v52, v188, v52
	v_exp_f32_e32 v192, v37
	v_fma_f32 v37, v172, v40, -v133
	v_add_f32_e32 v36, v189, v52
	v_exp_f32_e32 v193, v37
	v_fma_f32 v37, v172, v41, -v133
	v_add_f32_e32 v36, v190, v36
	v_exp_f32_e32 v194, v37
	v_fma_f32 v37, v172, v42, -v133
	v_add_f32_e32 v36, v191, v36
	v_exp_f32_e32 v195, v37
	v_fma_f32 v37, v172, v43, -v133
	v_add_f32_e32 v36, v192, v36
	v_exp_f32_e32 v196, v37
	v_fma_f32 v37, v172, v44, -v133
	v_add_f32_e32 v36, v193, v36
	v_exp_f32_e32 v197, v37
	v_fma_f32 v37, v172, v45, -v133
	v_add_f32_e32 v36, v194, v36
	v_exp_f32_e32 v198, v37
	v_fma_f32 v37, v172, v46, -v133
	v_add_f32_e32 v36, v195, v36
	v_exp_f32_e32 v199, v37
	v_fma_f32 v37, v172, v47, -v133
	v_add_f32_e32 v36, v196, v36
	v_exp_f32_e32 v203, v37
	v_fma_f32 v37, v172, v48, -v133
	v_add_f32_e32 v36, v197, v36
	v_exp_f32_e32 v204, v37
	v_fma_f32 v37, v172, v49, -v133
	v_add_f32_e32 v36, v198, v36
	v_exp_f32_e32 v205, v37
	v_fma_f32 v37, v172, v50, -v133
	v_add_f32_e32 v36, v199, v36
	v_exp_f32_e32 v206, v37
	v_fma_f32 v37, v172, v51, -v133
	v_add_f32_e32 v36, v203, v36
	v_exp_f32_e32 v207, v37
	v_fma_f32 v20, v172, v20, -v133
	v_add_f32_e32 v36, v204, v36
	v_exp_f32_e32 v20, v20
	v_fma_f32 v21, v172, v21, -v133
	v_add_f32_e32 v36, v205, v36
	v_exp_f32_e32 v21, v21
	v_fma_f32 v22, v172, v22, -v133
	v_add_f32_e32 v36, v206, v36
	v_exp_f32_e32 v22, v22
	v_fma_f32 v23, v172, v23, -v133
	v_add_f32_e32 v36, v207, v36
	v_exp_f32_e32 v23, v23
	v_fma_f32 v24, v172, v24, -v133
	v_add_f32_e32 v36, v20, v36
	v_exp_f32_e32 v24, v24
	v_fma_f32 v25, v172, v25, -v133
	v_add_f32_e32 v36, v21, v36
	v_exp_f32_e32 v25, v25
	v_fma_f32 v26, v172, v26, -v133
	v_add_f32_e32 v36, v22, v36
	v_exp_f32_e32 v26, v26
	v_fma_f32 v27, v172, v27, -v133
	v_add_f32_e32 v36, v23, v36
	v_exp_f32_e32 v27, v27
	v_fma_f32 v28, v172, v28, -v133
	v_add_f32_e32 v36, v24, v36
	v_exp_f32_e32 v28, v28
	v_fma_f32 v29, v172, v29, -v133
	v_add_f32_e32 v36, v25, v36
	v_exp_f32_e32 v29, v29
	v_fma_f32 v30, v172, v30, -v133
	v_add_f32_e32 v36, v26, v36
	v_exp_f32_e32 v30, v30
	v_fma_f32 v31, v172, v31, -v133
	v_add_f32_e32 v36, v27, v36
	v_exp_f32_e32 v31, v31
	v_fma_f32 v32, v172, v32, -v133
	v_add_f32_e32 v36, v28, v36
	v_exp_f32_e32 v32, v32
	v_fma_f32 v33, v172, v33, -v133
	v_add_f32_e32 v36, v29, v36
	v_exp_f32_e32 v33, v33
	v_fma_f32 v34, v172, v34, -v133
	v_add_f32_e32 v36, v30, v36
	v_exp_f32_e32 v34, v34
	v_fma_f32 v35, v172, v35, -v133
	v_add_f32_e32 v36, v31, v36
	v_exp_f32_e32 v35, v35
	v_fma_f32 v4, v172, v4, -v133
	v_add_f32_e32 v36, v32, v36
	v_exp_f32_e32 v4, v4
	v_fma_f32 v5, v172, v5, -v133
	v_add_f32_e32 v36, v33, v36
	v_exp_f32_e32 v5, v5
	v_fma_f32 v6, v172, v6, -v133
	v_add_f32_e32 v36, v34, v36
	v_exp_f32_e32 v6, v6
	v_fma_f32 v7, v172, v7, -v133
	v_add_f32_e32 v36, v35, v36
	v_exp_f32_e32 v7, v7
	v_fma_f32 v8, v172, v8, -v133
	v_add_f32_e32 v36, v4, v36
	v_exp_f32_e32 v8, v8
	v_fma_f32 v9, v172, v9, -v133
	v_add_f32_e32 v36, v5, v36
	v_exp_f32_e32 v9, v9
	v_fma_f32 v10, v172, v10, -v133
	v_add_f32_e32 v36, v6, v36
	v_exp_f32_e32 v10, v10
	v_fma_f32 v11, v172, v11, -v133
	v_add_f32_e32 v36, v7, v36
	v_exp_f32_e32 v11, v11
	v_fma_f32 v12, v172, v12, -v133
	v_add_f32_e32 v36, v8, v36
	v_exp_f32_e32 v12, v12
	v_fma_f32 v13, v172, v13, -v133
	v_add_f32_e32 v36, v9, v36
	v_exp_f32_e32 v13, v13
	v_fma_f32 v14, v172, v14, -v133
	v_add_f32_e32 v36, v10, v36
	v_exp_f32_e32 v14, v14
	v_fma_f32 v15, v172, v15, -v133
	v_add_f32_e32 v36, v11, v36
	v_exp_f32_e32 v15, v15
	v_fma_f32 v16, v172, v16, -v133
	v_add_f32_e32 v36, v12, v36
	v_exp_f32_e32 v16, v16
	v_fma_f32 v17, v172, v17, -v133
	v_add_f32_e32 v36, v13, v36
	v_exp_f32_e32 v17, v17
	v_fma_f32 v18, v172, v18, -v133
	v_add_f32_e32 v36, v14, v36
	v_exp_f32_e32 v18, v18
	v_sub_f32_e32 v37, v132, v133
	v_add_f32_e32 v36, v15, v36
	v_exp_f32_e32 v132, v37
	v_add_f32_e32 v36, v16, v36
	v_add_f32_e32 v36, v17, v36
	v_add_f32_e32 v36, v18, v36
	v_add_f32_e32 v36, v132, v36
	ds_bpermute_b32 v37, v134, v36
	v_cvt_pk_bf16_f32 v59, v98, v99
	v_cvt_pk_bf16_f32 v98, v16, v17
	v_lshl_add_u64 v[16:17], v[158:159], 0, s[12:13]
	v_cvt_pk_bf16_f32 v56, v92, v93
	v_cvt_pk_bf16_f32 v92, v4, v5
	v_lshl_add_u64 v[4:5], v[16:17], 0, v[160:161]
	s_or_b32 s12, s4, 64
	v_cvt_pk_bf16_f32 v57, v94, v95
	v_cvt_pk_bf16_f32 v93, v6, v7
	v_cvt_pk_bf16_f32 v94, v8, v9
	global_load_dwordx4 v[4:7], v[4:5], off
	v_lshl_add_u64 v[8:9], v[16:17], 0, v[162:163]
	s_ashr_i32 s13, s12, 31
	v_cvt_pk_bf16_f32 v58, v96, v97
	v_cvt_pk_bf16_f32 v95, v10, v11
	v_cvt_pk_bf16_f32 v96, v12, v13
	global_load_dwordx4 v[8:11], v[8:9], off
	v_lshl_add_u64 v[12:13], v[16:17], 0, v[164:165]
	s_lshl_b64 s[12:13], s[12:13], 9
	v_cvt_pk_bf16_f32 v55, v90, v91
	v_cvt_pk_bf16_f32 v90, v32, v33
	v_cvt_pk_bf16_f32 v97, v14, v15
	global_load_dwordx4 v[12:15], v[12:13], off
	v_lshl_add_u64 v[16:17], v[16:17], 0, v[166:167]
	v_lshl_add_u64 v[32:33], v[158:159], 0, s[12:13]
	s_waitcnt lgkmcnt(0)
	v_add_f32_e32 v131, v36, v37
	v_cvt_pk_bf16_f32 v36, v19, v116
	v_cvt_pk_bf16_f32 v52, v84, v85
	v_cvt_pk_bf16_f32 v84, v20, v21
	v_cvt_pk_bf16_f32 v99, v18, v132
	global_load_dwordx4 v[16:19], v[16:17], off
	v_lshl_add_u64 v[20:21], v[32:33], 0, v[160:161]
	v_cvt_pk_bf16_f32 v53, v86, v87
	v_cvt_pk_bf16_f32 v85, v22, v23
	v_cvt_pk_bf16_f32 v86, v24, v25
	global_load_dwordx4 v[20:23], v[20:21], off
	v_lshl_add_u64 v[24:25], v[32:33], 0, v[162:163]
	v_cvt_pk_bf16_f32 v54, v88, v89
	v_cvt_pk_bf16_f32 v87, v26, v27
	v_cvt_pk_bf16_f32 v88, v28, v29
	global_load_dwordx4 v[24:27], v[24:25], off
	v_lshl_add_u64 v[28:29], v[32:33], 0, v[164:165]
	v_cvt_pk_bf16_f32 v89, v30, v31
	global_load_dwordx4 v[28:31], v[28:29], off
	v_lshl_add_u64 v[32:33], v[32:33], 0, v[166:167]
	v_cvt_pk_bf16_f32 v91, v34, v35
	global_load_dwordx4 v[32:35], v[32:33], off
	s_or_b32 s12, s4, 0x80
	s_ashr_i32 s13, s12, 31
	s_lshl_b64 s[12:13], s[12:13], 9
	v_lshl_add_u64 v[220:221], v[158:159], 0, s[12:13]
	v_lshl_add_u64 v[208:209], v[220:221], 0, v[160:161]
	s_or_b32 s4, s4, 0xc0
	global_load_dwordx4 v[208:211], v[208:209], off
	v_lshl_add_u64 v[212:213], v[220:221], 0, v[162:163]
	s_ashr_i32 s5, s4, 31
	global_load_dwordx4 v[212:215], v[212:213], off
	v_lshl_add_u64 v[216:217], v[220:221], 0, v[164:165]
	s_lshl_b64 s[4:5], s[4:5], 9
	global_load_dwordx4 v[216:219], v[216:217], off
	v_lshl_add_u64 v[220:221], v[220:221], 0, v[166:167]
	v_lshl_add_u64 v[236:237], v[158:159], 0, s[4:5]
	global_load_dwordx4 v[220:223], v[220:221], off
	v_lshl_add_u64 v[224:225], v[236:237], 0, v[160:161]
	global_load_dwordx4 v[224:227], v[224:225], off
	v_lshl_add_u64 v[228:229], v[236:237], 0, v[162:163]
	global_load_dwordx4 v[228:231], v[228:229], off
	v_lshl_add_u64 v[232:233], v[236:237], 0, v[164:165]
	global_load_dwordx4 v[232:235], v[232:233], off
	v_lshl_add_u64 v[236:237], v[236:237], 0, v[166:167]
	global_load_dwordx4 v[236:239], v[236:237], off
	s_waitcnt vmcnt(15)
	ds_write_b128 v179, v[4:7]
	s_waitcnt vmcnt(14)
	ds_write_b128 v179, v[8:11] offset:8448
	s_waitcnt vmcnt(13)
	ds_write_b128 v179, v[12:15] offset:16896
	s_waitcnt vmcnt(12)
	ds_write_b128 v179, v[16:19] offset:25344
	s_waitcnt vmcnt(11)
	ds_write_b128 v179, v[20:23] offset:33792
	s_waitcnt vmcnt(10)
	ds_write_b128 v179, v[24:27] offset:42240
	s_waitcnt vmcnt(9)
	ds_write_b128 v179, v[28:31] offset:50688
	s_waitcnt vmcnt(8)
	ds_write_b128 v179, v[32:35] offset:59136
	s_waitcnt vmcnt(7)
	ds_write_b128 v180, v[208:211]
	s_waitcnt vmcnt(6)
	ds_write_b128 v180, v[212:215] offset:8448
	s_waitcnt vmcnt(5)
	ds_write_b128 v180, v[216:219] offset:16896
	s_waitcnt vmcnt(4)
	ds_write_b128 v180, v[220:223] offset:25344
	s_waitcnt vmcnt(3)
	ds_write_b128 v181, v[224:227]
	s_waitcnt vmcnt(2)
	ds_write_b128 v181, v[228:231] offset:8448
	s_waitcnt vmcnt(1)
	ds_write_b128 v181, v[232:235] offset:16896
	s_waitcnt vmcnt(0)
	ds_write_b128 v181, v[236:239] offset:25344
	v_div_scale_f32 v4, s[4:5], v131, v131, 1.0
	v_rcp_f32_e32 v5, v4
	v_cvt_pk_bf16_f32 v44, v100, v101
	v_cvt_pk_bf16_f32 v37, v117, v118
	v_cvt_pk_bf16_f32 v38, v119, v120
	v_fma_f32 v6, -v4, v5, 1.0
	v_fmac_f32_e32 v5, v6, v5
	v_div_scale_f32 v6, vcc, 1.0, v131, 1.0
	v_mul_f32_e32 v7, v6, v5
	v_fma_f32 v8, -v4, v7, v6
	v_fmac_f32_e32 v7, v8, v5
	v_fma_f32 v4, -v4, v7, v6
	v_div_fmas_f32 v4, v4, v5, v7
	v_div_fixup_f32 v100, v4, v131, 1.0
	v_lshl_add_u64 v[4:5], v[170:171], 0, s[18:19]
	v_cvt_pk_bf16_f32 v39, v121, v122
	v_cvt_pk_bf16_f32 v40, v123, v124
	v_cvt_pk_bf16_f32 v41, v125, v126
	v_cvt_pk_bf16_f32 v42, v127, v128
	v_cvt_pk_bf16_f32 v43, v129, v130
	v_cvt_pk_bf16_f32 v45, v102, v103
	v_cvt_pk_bf16_f32 v46, v104, v105
	v_cvt_pk_bf16_f32 v47, v106, v107
	v_cvt_pk_bf16_f32 v48, v108, v109
	v_cvt_pk_bf16_f32 v49, v110, v111
	v_cvt_pk_bf16_f32 v50, v112, v113
	v_cvt_pk_bf16_f32 v51, v114, v115
	v_cvt_pk_bf16_f32 v60, v68, v69
	v_cvt_pk_bf16_f32 v61, v70, v71
	v_cvt_pk_bf16_f32 v62, v72, v73
	v_cvt_pk_bf16_f32 v63, v74, v75
	v_cvt_pk_bf16_f32 v64, v76, v77
	v_cvt_pk_bf16_f32 v65, v78, v79
	v_cvt_pk_bf16_f32 v66, v80, v81
	v_cvt_pk_bf16_f32 v67, v82, v83
	v_cvt_pk_bf16_f32 v68, v135, v136
	v_cvt_pk_bf16_f32 v69, v137, v138
	v_cvt_pk_bf16_f32 v70, v139, v140
	v_cvt_pk_bf16_f32 v71, v141, v142
	v_cvt_pk_bf16_f32 v72, v143, v144
	v_cvt_pk_bf16_f32 v73, v145, v146
	v_cvt_pk_bf16_f32 v74, v147, v174
	v_cvt_pk_bf16_f32 v75, v175, v188
	v_cvt_pk_bf16_f32 v76, v189, v190
	v_cvt_pk_bf16_f32 v77, v191, v192
	v_cvt_pk_bf16_f32 v78, v193, v194
	v_cvt_pk_bf16_f32 v79, v195, v196
	v_cvt_pk_bf16_f32 v80, v197, v198
	v_cvt_pk_bf16_f32 v81, v199, v203
	v_cvt_pk_bf16_f32 v82, v204, v205
	v_cvt_pk_bf16_f32 v83, v206, v207
	v_mov_b32_e32 v101, v100
	v_lshl_add_u64 v[102:103], v[168:169], 0, v[4:5]
	s_waitcnt lgkmcnt(0)
	s_barrier
